# mix_unit: one static priority raise for waves 0-3 at the unit loop entry (reset at its exit), on top of the attention one
# baseline (speedup 1.0000x reference)
.LBB0_367:
	v_mov_b32_e32 v93, v0
	v_readlane_b32 s0, v251, 36
	s_cmp_gt_u32 s0, 3
	s_cbranch_scc1 .Lprio_mx
	s_setprio 1
.Lprio_mx:
	s_lshl_b32 s90, s55, 5
	s_waitcnt vmcnt(0)
	v_mov_b64_e32 v[2:3], s[10:11]
	v_ashrrev_i32_e32 v95, 4, v93
	v_and_b32_e32 v94, 15, v93
	v_add_u32_e32 v4, s90, v95
	v_mad_i64_i32 v[2:3], s[0:1], v4, s96, v[2:3]
	v_lshlrev_b32_e32 v114, 4, v94
	v_mov_b32_e32 v1, v224
	v_readlane_b32 s91, v251, 36
	v_lshl_add_u64 v[2:3], v[2:3], 0, v[114:115]
	global_load_dwordx4 v[50:53], v[2:3], off
	v_cmp_gt_u32_e64 s[50:51], 8, v94
	v_mov_b32_e32 v30, 0
	v_mov_b32_e32 v54, 0
	v_mov_b32_e32 v55, 0
	v_mov_b32_e32 v56, 0
	v_mov_b32_e32 v57, 0
	s_and_saveexec_b64 s[0:1], s[50:51]
	s_cbranch_execz .LBB0_369
	global_load_dwordx4 v[54:57], v[2:3], off offset:256

.LBB0_412:
	s_setprio 0
	v_readlane_b32 s0, v253, 23
	v_readlane_b32 s1, v253, 24
	v_readlane_b32 s76, v254, 60
	s_andn2_b64 vcc, exec, s[0:1]
	v_readlane_b32 s77, v254, 61
	s_cbranch_vccnz .LBB0_421
	v_readlane_b32 s0, v254, 51
	s_lshl_b32 s2, s0, 8
	s_mov_b32 s3, s76
	s_branch .LBB0_416
